# prep32 B3 (LoRA MFMA stage) rewritten wave-uniform with register-resident lin fragments, rotated tile start per unit; rwkv_pre S2 reads hoisted
# baseline (speedup 1.0000x reference)
.LBB0_260:
	v_or_b32_e32 v0, s76, v180
	s_movk_i32 s2, 0x600
	v_mad_i64_i32 v[154:155], s[0:1], v0, s95, 0
	v_mad_i64_i32 v[156:157], s[0:1], v0, s2, 0
	v_or_b32_e32 v0, 16, v0
	v_mad_i64_i32 v[158:159], s[0:1], v0, s95, 0
	v_mad_i64_i32 v[160:161], s[0:1], v0, s2, 0
	s_mov_b32 s31, 0
	v_mov_b32_e32 v162, v230
	s_waitcnt lgkmcnt(0)
	s_barrier
	v_readlane_b32 s2, v251, 12
	v_readlane_b32 s10, v253, 60
	v_mbcnt_lo_u32_b32 v98, -1, 0
	v_mbcnt_hi_u32_b32 v98, -1, v98
	s_lshr_b32 s2, s2, 6
	s_mul_i32 s22, s2, 15
	s_mul_hi_u32 s23, s74, 0x11111112
	s_mul_i32 s23, s23, 15
	s_sub_u32 s23, s74, s23
	s_add_u32 s4, s22, s23
	s_add_u32 s23, s22, 15
	s_mul_i32 s7, s10, 0x78000
	s_add_u32 s0, s36, 0x55484800
	s_addc_u32 s1, s37, 0
	s_add_u32 s0, s0, s7
	s_addc_u32 s1, s1, 0
	v_and_b32_e32 v99, 15, v98
	v_lshrrev_b32_e32 v100, 4, v98
	v_lshlrev_b32_e32 v159, 4, v100
	v_lshl_add_u32 v153, v99, 8, v159
	v_mul_u32_u24_e32 v0, 0x210, v99
	s_mov_b32 s7, 0x17600
	v_add3_u32 v0, v0, v159, s7
	ds_read_b128 v[38:41], v0 offset:0
	ds_read_b128 v[42:45], v0 offset:64
	ds_read_b128 v[46:49], v0 offset:8448
	ds_read_b128 v[50:53], v0 offset:8512
	ds_read_b128 v[54:57], v0 offset:128
	ds_read_b128 v[58:61], v0 offset:192
	ds_read_b128 v[62:65], v0 offset:8576
	ds_read_b128 v[66:69], v0 offset:8640
	ds_read_b128 v[70:73], v0 offset:256
	ds_read_b128 v[74:77], v0 offset:320
	ds_read_b128 v[78:81], v0 offset:384
	ds_read_b128 v[82:85], v0 offset:448
	ds_read_b128 v[86:89], v0 offset:8704
	ds_read_b128 v[90:93], v0 offset:8768
	ds_read_b128 v[94:97], v0 offset:8832
	ds_read_b128 v[2:5], v0 offset:8896
	v_mul_u32_u24_e32 v154, 0x300, v99
	v_lshlrev_b32_e32 v102, 3, v100
	s_mov_b32 s7, 0x1b800
	v_add3_u32 v154, v154, v102, s7
	v_or_b32_e32 v103, s76, v99
	v_mul_u32_u24_e32 v155, 0x600, v103
	v_add_u32_e32 v155, v155, v159
	v_add_u32_e32 v156, 0x6000, v155
	v_mul_u32_u24_e32 v157, 0x300, v103
	v_add_u32_e32 v157, v157, v102
	v_add_u32_e32 v158, 0x3000, v157
	s_mov_b32 s3, 0
	s_mov_b32 s7, s4
	s_mul_hi_u32 s8, s7, 0xaaaaaab
	s_mul_i32 s10, s8, 24
	s_sub_u32 s10, s7, s10
	s_lshl_b32 s12, s7, 12
	s_add_u32 s16, s0, s12
	s_addc_u32 s17, s1, 0
	global_load_dwordx4 v[6:9], v153, s[16:17] offset:0
	global_load_dwordx4 v[10:13], v153, s[16:17] offset:64
	global_load_dwordx4 v[14:17], v153, s[16:17] offset:128
	global_load_dwordx4 v[18:21], v153, s[16:17] offset:192
	s_cmp_gt_u32 s8, 3
	s_cbranch_scc1 .Lb3_nb_init
	s_cmp_lt_u32 s8, 2
	s_cselect_b32 s18, s68, s70
	s_cselect_b32 s19, s69, s71
	s_and_b32 s12, s8, 1
	s_mul_i32 s12, s12, 0x600
	s_lshl_b32 s14, s10, 6
	s_add_u32 s12, s12, s14
	s_add_u32 s18, s18, s12
	s_addc_u32 s19, s19, 0
	global_load_dwordx4 v[22:25], v159, s[18:19]
.Lb3_nb_init:
	s_waitcnt vmcnt(0) lgkmcnt(0)
.Lb3_tile:
	s_mul_hi_u32 s5, s4, 0xaaaaaab
	s_mul_i32 s6, s5, 24
	s_sub_u32 s6, s4, s6
	v_mov_b64_e32 v[104:105], v[22:23]
	v_mov_b64_e32 v[106:107], v[24:25]
	s_cmp_gt_u32 s5, 3
	s_cbranch_scc1 .Lb3_gate
	s_cmp_gt_u32 s5, 1
	s_cbranch_scc1 .Lb3_iclr
	v_mfma_f32_16x16x32_bf16 v[26:29], v[6:9], v[38:41], 0
	v_mfma_f32_16x16x32_bf16 v[26:29], v[10:13], v[42:45], v[26:29]
	v_mfma_f32_16x16x32_bf16 v[30:33], v[6:9], v[46:49], 0
	v_mfma_f32_16x16x32_bf16 v[30:33], v[10:13], v[50:53], v[30:33]
	s_mul_i32 s12, s5, 0x1800000
	s_lshl_b32 s14, s6, 6
	s_add_u32 s20, s56, s12
	s_addc_u32 s21, s57, 0
	s_add_u32 s20, s20, s14
	s_addc_u32 s21, s21, 0
	s_add_i32 s7, s4, 1
	s_cmp_eq_u32 s7, s23
	s_cselect_b32 s7, s22, s7
	s_cmp_eq_u32 s3, 14
	s_cbranch_scc1 .Lb3_skip_d
	s_mul_hi_u32 s8, s7, 0xaaaaaab
	s_mul_i32 s10, s8, 24
	s_sub_u32 s10, s7, s10
	s_lshl_b32 s12, s7, 12
	s_add_u32 s16, s0, s12
	s_addc_u32 s17, s1, 0
	global_load_dwordx4 v[6:9], v153, s[16:17] offset:0
	global_load_dwordx4 v[10:13], v153, s[16:17] offset:64
	global_load_dwordx4 v[14:17], v153, s[16:17] offset:128
	global_load_dwordx4 v[18:21], v153, s[16:17] offset:192
	s_cmp_gt_u32 s8, 3
	s_cbranch_scc1 .Lb3_nb_d
	s_cmp_lt_u32 s8, 2
	s_cselect_b32 s18, s68, s70
	s_cselect_b32 s19, s69, s71
	s_and_b32 s12, s8, 1
	s_mul_i32 s12, s12, 0x600
	s_lshl_b32 s14, s10, 6
	s_add_u32 s12, s12, s14
	s_add_u32 s18, s18, s12
	s_addc_u32 s19, s19, 0
	global_load_dwordx4 v[22:25], v159, s[18:19]
.Lb3_nb_d:
.Lb3_skip_d:
	v_pk_add_f32 v[26:27], v[26:27], v[104:105]
	v_pk_add_f32 v[28:29], v[28:29], v[106:107]
	v_mul_f32_e32 v160, 0xbfb8aa3b, v26
	v_mul_f32_e32 v161, 0xbfb8aa3b, v27
	v_mul_f32_e32 v162, 0xbfb8aa3b, v28
	v_mul_f32_e32 v163, 0xbfb8aa3b, v29
	v_exp_f32_e32 v160, v160
	v_exp_f32_e32 v161, v161
	v_exp_f32_e32 v162, v162
	v_exp_f32_e32 v163, v163
	v_add_f32_e32 v160, 1.0, v160
	v_add_f32_e32 v161, 1.0, v161
	v_add_f32_e32 v162, 1.0, v162
	v_add_f32_e32 v163, 1.0, v163
	v_rcp_f32_e32 v160, v160
	v_rcp_f32_e32 v161, v161
	v_rcp_f32_e32 v162, v162
	v_rcp_f32_e32 v163, v163
	v_mul_f32_e32 v160, 0xbf1b4598, v160
	v_mul_f32_e32 v161, 0xbf1b4598, v161
	v_mul_f32_e32 v162, 0xbf1b4598, v162
	v_mul_f32_e32 v163, 0xbf1b4598, v163
	global_store_dwordx4 v155, v[160:163], s[20:21]
	v_pk_add_f32 v[30:31], v[30:31], v[104:105]
	v_pk_add_f32 v[32:33], v[32:33], v[106:107]
	v_mul_f32_e32 v164, 0xbfb8aa3b, v30
	v_mul_f32_e32 v165, 0xbfb8aa3b, v31
	v_mul_f32_e32 v166, 0xbfb8aa3b, v32
	v_mul_f32_e32 v167, 0xbfb8aa3b, v33
	v_exp_f32_e32 v164, v164
	v_exp_f32_e32 v165, v165
	v_exp_f32_e32 v166, v166
	v_exp_f32_e32 v167, v167
	v_add_f32_e32 v164, 1.0, v164
	v_add_f32_e32 v165, 1.0, v165
	v_add_f32_e32 v166, 1.0, v166
	v_add_f32_e32 v167, 1.0, v167
	v_rcp_f32_e32 v164, v164
	v_rcp_f32_e32 v165, v165
	v_rcp_f32_e32 v166, v166
	v_rcp_f32_e32 v167, v167
	v_mul_f32_e32 v164, 0xbf1b4598, v164
	v_mul_f32_e32 v165, 0xbf1b4598, v165
	v_mul_f32_e32 v166, 0xbf1b4598, v166
	v_mul_f32_e32 v167, 0xbf1b4598, v167
	global_store_dwordx4 v156, v[164:167], s[20:21]
	s_waitcnt vmcnt(2)
	s_branch .Lb3_next
.Lb3_iclr:
	v_mfma_f32_16x16x32_bf16 v[26:29], v[6:9], v[54:57], 0
	v_mfma_f32_16x16x32_bf16 v[26:29], v[10:13], v[58:61], v[26:29]
	v_mfma_f32_16x16x32_bf16 v[30:33], v[6:9], v[62:65], 0
	v_mfma_f32_16x16x32_bf16 v[30:33], v[10:13], v[66:69], v[30:33]
	s_sub_u32 s12, s5, 2
	s_mul_i32 s12, s12, 0x6000
	s_lshl_b32 s14, s6, 5
	s_add_u32 s12, s12, s14
	v_add_u32_e32 v108, s12, v154
	s_add_i32 s7, s4, 1
	s_cmp_eq_u32 s7, s23
	s_cselect_b32 s7, s22, s7
	s_cmp_eq_u32 s3, 14
	s_cbranch_scc1 .Lb3_skip_i
	s_mul_hi_u32 s8, s7, 0xaaaaaab
	s_mul_i32 s10, s8, 24
	s_sub_u32 s10, s7, s10
	s_lshl_b32 s12, s7, 12
	s_add_u32 s16, s0, s12
	s_addc_u32 s17, s1, 0
	global_load_dwordx4 v[6:9], v153, s[16:17] offset:0
	global_load_dwordx4 v[10:13], v153, s[16:17] offset:64
	global_load_dwordx4 v[14:17], v153, s[16:17] offset:128
	global_load_dwordx4 v[18:21], v153, s[16:17] offset:192
	s_cmp_gt_u32 s8, 3
	s_cbranch_scc1 .Lb3_nb_i
	s_cmp_lt_u32 s8, 2
	s_cselect_b32 s18, s68, s70
	s_cselect_b32 s19, s69, s71
	s_and_b32 s12, s8, 1
	s_mul_i32 s12, s12, 0x600
	s_lshl_b32 s14, s10, 6
	s_add_u32 s12, s12, s14
	s_add_u32 s18, s18, s12
	s_addc_u32 s19, s19, 0
	global_load_dwordx4 v[22:25], v159, s[18:19]
.Lb3_nb_i:
.Lb3_skip_i:
	v_pk_add_f32 v[26:27], v[26:27], v[104:105]
	v_pk_add_f32 v[28:29], v[28:29], v[106:107]
	v_mul_f32_e32 v160, 0xbfb8aa3b, v26
	v_mul_f32_e32 v161, 0xbfb8aa3b, v27
	v_mul_f32_e32 v162, 0xbfb8aa3b, v28
	v_mul_f32_e32 v163, 0xbfb8aa3b, v29
	v_exp_f32_e32 v160, v160
	v_exp_f32_e32 v161, v161
	v_exp_f32_e32 v162, v162
	v_exp_f32_e32 v163, v163
	v_add_f32_e32 v160, 1.0, v160
	v_add_f32_e32 v161, 1.0, v161
	v_add_f32_e32 v162, 1.0, v162
	v_add_f32_e32 v163, 1.0, v163
	v_rcp_f32_e32 v160, v160
	v_rcp_f32_e32 v161, v161
	v_rcp_f32_e32 v162, v162
	v_rcp_f32_e32 v163, v163
	s_nop 0
	v_cvt_pk_bf16_f32 v160, v160, v161
	v_cvt_pk_bf16_f32 v161, v162, v163
	ds_write_b64 v108, v[160:161] offset:0
	v_pk_add_f32 v[30:31], v[30:31], v[104:105]
	v_pk_add_f32 v[32:33], v[32:33], v[106:107]
	v_mul_f32_e32 v164, 0xbfb8aa3b, v30
	v_mul_f32_e32 v165, 0xbfb8aa3b, v31
	v_mul_f32_e32 v166, 0xbfb8aa3b, v32
	v_mul_f32_e32 v167, 0xbfb8aa3b, v33
	v_exp_f32_e32 v164, v164
	v_exp_f32_e32 v165, v165
	v_exp_f32_e32 v166, v166
	v_exp_f32_e32 v167, v167
	v_add_f32_e32 v164, 1.0, v164
	v_add_f32_e32 v165, 1.0, v165
	v_add_f32_e32 v166, 1.0, v166
	v_add_f32_e32 v167, 1.0, v167
	v_rcp_f32_e32 v164, v164
	v_rcp_f32_e32 v165, v165
	v_rcp_f32_e32 v166, v166
	v_rcp_f32_e32 v167, v167
	s_nop 0
	v_cvt_pk_bf16_f32 v164, v164, v165
	v_cvt_pk_bf16_f32 v165, v166, v167
	ds_write_b64 v108, v[164:165] offset:12288
	s_waitcnt vmcnt(0)
	s_branch .Lb3_next
.Lb3_gate:
	v_mfma_f32_16x16x32_bf16 v[26:29], v[6:9], v[70:73], 0
	v_mfma_f32_16x16x32_bf16 v[26:29], v[10:13], v[74:77], v[26:29]
	v_mfma_f32_16x16x32_bf16 v[26:29], v[14:17], v[78:81], v[26:29]
	v_mfma_f32_16x16x32_bf16 v[26:29], v[18:21], v[82:85], v[26:29]
	v_mfma_f32_16x16x32_bf16 v[30:33], v[6:9], v[86:89], 0
	v_mfma_f32_16x16x32_bf16 v[30:33], v[10:13], v[90:93], v[30:33]
	v_mfma_f32_16x16x32_bf16 v[30:33], v[14:17], v[94:97], v[30:33]
	v_mfma_f32_16x16x32_bf16 v[30:33], v[18:21], v[2:5], v[30:33]
	s_lshl_b32 s14, s6, 5
	s_add_u32 s20, s54, s14
	s_addc_u32 s21, s55, 0
	s_add_i32 s7, s4, 1
	s_cmp_eq_u32 s7, s23
	s_cselect_b32 s7, s22, s7
	s_cmp_eq_u32 s3, 14
	s_cbranch_scc1 .Lb3_skip_g
	s_mul_hi_u32 s8, s7, 0xaaaaaab
	s_mul_i32 s10, s8, 24
	s_sub_u32 s10, s7, s10
	s_lshl_b32 s12, s7, 12
	s_add_u32 s16, s0, s12
	s_addc_u32 s17, s1, 0
	global_load_dwordx4 v[6:9], v153, s[16:17] offset:0
	global_load_dwordx4 v[10:13], v153, s[16:17] offset:64
	global_load_dwordx4 v[14:17], v153, s[16:17] offset:128
	global_load_dwordx4 v[18:21], v153, s[16:17] offset:192
	s_cmp_gt_u32 s8, 3
	s_cbranch_scc1 .Lb3_nb_g
	s_cmp_lt_u32 s8, 2
	s_cselect_b32 s18, s68, s70
	s_cselect_b32 s19, s69, s71
	s_and_b32 s12, s8, 1
	s_mul_i32 s12, s12, 0x600
	s_lshl_b32 s14, s10, 6
	s_add_u32 s12, s12, s14
	s_add_u32 s18, s18, s12
	s_addc_u32 s19, s19, 0
	global_load_dwordx4 v[22:25], v159, s[18:19]
.Lb3_nb_g:
.Lb3_skip_g:
	v_cvt_pk_bf16_f32 v160, v26, v27
	v_cvt_pk_bf16_f32 v161, v28, v29
	global_store_dwordx2 v157, v[160:161], s[20:21]
	v_cvt_pk_bf16_f32 v164, v30, v31
	v_cvt_pk_bf16_f32 v165, v32, v33
	global_store_dwordx2 v158, v[164:165], s[20:21]
	s_waitcnt vmcnt(2)
.Lb3_next:
	s_add_i32 s3, s3, 1
	s_mov_b32 s4, s7
	s_cmp_lt_u32 s3, 15
	s_cbranch_scc1 .Lb3_tile

.LBB0_622:
	v_mov_b32_e32 v18, v187
	s_waitcnt lgkmcnt(0)
	s_barrier
	v_readlane_b32 s2, v252, 43
	v_bfe_u32 v32, v18, 4, 2
	v_ashrrev_i32_e32 v0, 3, v18
	v_and_b32_e32 v19, 15, v18
	v_and_b32_e32 v33, -16, v0
	v_bfi_b32 v20, -16, v0, v18
	v_lshl_add_u32 v0, v32, 4, 0
	v_lshrrev_b32_e32 v18, 1, v18
	v_mad_u64_u32 v[30:31], s[0:1], v20, s40, v[0:1]
	v_and_b32_e32 v166, 32, v18
	v_readlane_b32 s0, v252, 41
	v_or_b32_e32 v167, v166, v19
	v_mad_u32_u24 v26, v167, s40, v0
	v_lshl_add_u32 v31, v19, 2, s0
	ds_read_b128 v[18:21], v30 offset:64512
	ds_read_b128 v[22:25], v26 offset:55296
	ds_read_b128 v[2:5], v30 offset:64576
	ds_read_b128 v[6:9], v26 offset:55360
	v_or_b32_e32 v10, 16, v167
	v_mad_u32_u24 v0, v10, s40, v0
	ds_read_b128 v[10:13], v0 offset:55296
	ds_read_b128 v[14:17], v0 offset:55360
	v_readlane_b32 s4, v252, 42
	s_mov_b32 s11, 0
	v_lshlrev_b32_e32 v175, 8, v33
	v_lshlrev_b32_e32 v174, 2, v166
	v_lshl_or_b32 v175, v32, 10, v175
	v_add3_u32 v31, v31, v174, v175
	s_waitcnt lgkmcnt(4)
	v_mfma_f32_16x16x32_bf16 v[176:179], v[18:21], v[22:25], 0
	s_waitcnt lgkmcnt(2)
	v_mfma_f32_16x16x32_bf16 v[176:179], v[2:5], v[6:9], v[176:179]
	s_waitcnt lgkmcnt(1)
	v_mfma_f32_16x16x32_bf16 v[240:243], v[18:21], v[10:13], 0
	s_waitcnt lgkmcnt(0)
	v_mfma_f32_16x16x32_bf16 v[240:243], v[2:5], v[14:17], v[240:243]
	s_nop 3
	ds_write_b32 v31, v176
	ds_write_b32 v31, v177 offset:256
	ds_write_b32 v31, v178 offset:512
	ds_write_b32 v31, v179 offset:768
	ds_write_b32 v31, v240 offset:64
	ds_write_b32 v31, v241 offset:320
	ds_write_b32 v31, v242 offset:576
	ds_write_b32 v31, v243 offset:832
	v_mov_b32_e32 v18, v187
	s_waitcnt lgkmcnt(0)
	s_barrier
	v_mov_b32_e32 v22, s2
	v_ashrrev_i32_e32 v20, 6, v18
	v_and_b32_e32 v21, 15, v18
	v_cmp_gt_i32_e64 s[0:1], 2, v20
	v_cmp_gt_i32_e32 vcc, 4, v20
	v_lshlrev_b32_e32 v20, 4, v20
	v_mov_b32_e32 v23, s96
	v_and_or_b32 v20, v20, 48, v21
	v_cndmask_b32_e32 v24, v22, v23, vcc
	v_mul_u32_u24_e32 v20, 0x90, v20
	v_and_b32_e32 v25, 48, v18
	v_and_b32_e32 v19, 63, v18
	v_add3_u32 v166, v24, v20, v25
	v_lshlrev_b32_e32 v20, 7, v18
	v_and_b32_e32 v24, 0xffffffc0, v18
	v_cmp_lt_u32_e64 s[2:3], 63, v18
	v_cmp_gt_u32_e32 vcc, 64, v18
	v_and_b32_e32 v18, 0x3fffffc0, v18
	v_lshlrev_b32_e32 v0, 2, v19
	v_and_b32_e32 v20, 0x1800, v20
	v_lshlrev_b32_e32 v18, 2, v18
	v_add_u32_e32 v20, s4, v20
	v_lshlrev_b32_e32 v26, 2, v21
	v_add3_u32 v168, s4, v0, v18
	v_cndmask_b32_e32 v18, v22, v23, vcc
	v_add3_u32 v167, v20, v24, v26
	v_mad_u32_u24 v169, v19, s40, v18
	v_mad_u32_u24 v170, v21, s40, v25
	v_lshlrev_b32_e32 v171, 1, v19
	s_branch .LBB0_625
